# weight-conversion stores (whole 128 B lines) write-through (sc1 nt) so the barrier's L2 write-back has less dirty data; on top of barrier + down-epilogue edits
# speedup vs baseline: 1.0065x; 1.0065x over previous
.LBB0_283:
	s_waitcnt vmcnt(0)
	v_mul_f32_e32 v60, 0x42800000, v60
	v_mul_f32_e32 v56, 0x42800000, v56
	v_med3_f32 v60, v60, s58, v153
	v_med3_f32 v56, v56, s58, v153
	v_mov_b32_e32 v155, v129
	v_cvt_pk_fp8_f32 v155, v60, v56
	v_mul_f32_e32 v52, 0x42800000, v52
	v_mul_f32_e32 v48, 0x42800000, v48
	v_med3_f32 v52, v52, s58, v153
	v_med3_f32 v48, v48, s58, v153
	v_cvt_pk_fp8_f32 v155, v52, v48 op_sel:[0,0,1]
	v_mul_f32_e32 v48, 0x42800000, v61
	v_mul_f32_e32 v52, 0x42800000, v57
	v_med3_f32 v48, v48, s58, v153
	v_med3_f32 v52, v52, s58, v153
	v_mov_b32_e32 v56, v129
	v_cvt_pk_fp8_f32 v56, v48, v52
	v_mul_f32_e32 v53, 0x42800000, v53
	v_mul_f32_e32 v49, 0x42800000, v49
	v_med3_f32 v48, v53, s58, v153
	v_med3_f32 v49, v49, s58, v153
	v_cvt_pk_fp8_f32 v56, v48, v49 op_sel:[0,0,1]
	v_mul_f32_e32 v48, 0x42800000, v62
	v_mul_f32_e32 v49, 0x42800000, v58
	v_med3_f32 v48, v48, s58, v153
	v_med3_f32 v49, v49, s58, v153
	v_mov_b32_e32 v53, v129
	v_cvt_pk_fp8_f32 v53, v48, v49
	v_mul_f32_e32 v52, 0x42800000, v54
	v_mul_f32_e32 v49, 0x42800000, v50
	v_med3_f32 v48, v52, s58, v153
	v_med3_f32 v49, v49, s58, v153
	v_cvt_pk_fp8_f32 v53, v48, v49 op_sel:[0,0,1]
	v_mul_f32_e32 v48, 0x42800000, v63
	v_mul_f32_e32 v49, 0x42800000, v59
	v_med3_f32 v48, v48, s58, v153
	v_med3_f32 v49, v49, s58, v153
	v_mov_b32_e32 v52, v129
	s_lshl_b32 s34, s59, 5
	s_lshl_b32 s28, s17, 7
	s_lshl_b64 s[48:49], s[48:49], 2
	v_cvt_pk_fp8_f32 v52, v48, v49
	s_add_u32 s46, s46, s48
	v_or_b32_e32 v64, s28, v132
	v_or_b32_e32 v66, s28, v133
	s_addc_u32 s47, s47, s49
	v_mad_i64_i32 v[64:65], s[48:49], s44, v64, 0
	s_ashr_i32 s35, s34, 31
	v_mad_i64_i32 v[66:67], s[50:51], s44, v66, 0
	v_mul_f32_e32 v50, 0x42800000, v55
	v_mul_f32_e32 v49, 0x42800000, v51
	v_lshl_add_u64 v[64:65], v[64:65], 2, s[46:47]
	s_lshl_b64 s[48:49], s[34:35], 2
	v_lshl_add_u64 v[66:67], v[66:67], 2, s[46:47]
	v_med3_f32 v48, v50, s58, v153
	v_med3_f32 v49, v49, s58, v153
	v_mul_f32_e32 v44, 0x42800000, v44
	v_mul_f32_e32 v40, 0x42800000, v40
	v_lshl_add_u64 v[64:65], v[64:65], 0, s[48:49]
	v_lshl_add_u64 v[66:67], v[66:67], 0, s[48:49]
	v_cvt_pk_fp8_f32 v52, v48, v49 op_sel:[0,0,1]
	v_med3_f32 v44, v44, s58, v153
	v_med3_f32 v40, v40, s58, v153
	v_mov_b32_e32 v48, v129
	v_lshl_add_u64 v[64:65], v[64:65], 0, v[128:129]
	v_lshl_add_u64 v[66:67], v[66:67], 0, v[128:129]
	v_cvt_pk_fp8_f32 v48, v44, v40
	global_load_dwordx4 v[116:119], v[64:65], off nt
	global_load_dwordx4 v[112:115], v[66:67], off nt
	v_or_b32_e32 v64, s28, v134
	v_or_b32_e32 v66, s28, v135
	v_mad_i64_i32 v[64:65], s[50:51], s44, v64, 0
	v_mad_i64_i32 v[66:67], s[50:51], s44, v66, 0
	v_mul_f32_e32 v36, 0x42800000, v36
	v_mul_f32_e32 v32, 0x42800000, v32
	v_lshl_add_u64 v[64:65], v[64:65], 2, s[46:47]
	v_lshl_add_u64 v[66:67], v[66:67], 2, s[46:47]
	v_med3_f32 v36, v36, s58, v153
	v_med3_f32 v32, v32, s58, v153
	v_lshl_add_u64 v[64:65], v[64:65], 0, s[48:49]
	v_lshl_add_u64 v[66:67], v[66:67], 0, s[48:49]
	v_cvt_pk_fp8_f32 v48, v36, v32 op_sel:[0,0,1]
	v_mul_f32_e32 v32, 0x42800000, v45
	v_mul_f32_e32 v36, 0x42800000, v41
	v_lshl_add_u64 v[64:65], v[64:65], 0, v[128:129]
	v_lshl_add_u64 v[66:67], v[66:67], 0, v[128:129]
	v_med3_f32 v32, v32, s58, v153
	v_med3_f32 v36, v36, s58, v153
	v_mov_b32_e32 v40, v129
	global_load_dwordx4 v[124:127], v[64:65], off nt
	global_load_dwordx4 v[120:123], v[66:67], off nt
	v_or_b32_e32 v64, s28, v136
	v_or_b32_e32 v66, s28, v137
	v_cvt_pk_fp8_f32 v40, v32, v36
	v_mad_i64_i32 v[64:65], s[50:51], s44, v64, 0
	v_mad_i64_i32 v[66:67], s[50:51], s44, v66, 0
	v_lshl_add_u64 v[64:65], v[64:65], 2, s[46:47]
	v_lshl_add_u64 v[66:67], v[66:67], 2, s[46:47]
	v_mul_f32_e32 v37, 0x42800000, v37
	v_mul_f32_e32 v33, 0x42800000, v33
	v_lshl_add_u64 v[64:65], v[64:65], 0, s[48:49]
	v_lshl_add_u64 v[66:67], v[66:67], 0, s[48:49]
	v_med3_f32 v32, v37, s58, v153
	v_med3_f32 v33, v33, s58, v153
	v_lshl_add_u64 v[64:65], v[64:65], 0, v[128:129]
	v_lshl_add_u64 v[66:67], v[66:67], 0, v[128:129]
	v_cvt_pk_fp8_f32 v40, v32, v33 op_sel:[0,0,1]
	v_mul_f32_e32 v32, 0x42800000, v46
	v_mul_f32_e32 v33, 0x42800000, v42
	global_load_dwordx4 v[100:103], v[64:65], off nt
	global_load_dwordx4 v[96:99], v[66:67], off nt
	v_or_b32_e32 v64, s28, v138
	v_or_b32_e32 v66, s28, v139
	v_med3_f32 v32, v32, s58, v153
	v_med3_f32 v33, v33, s58, v153
	v_mov_b32_e32 v37, v129
	v_mad_i64_i32 v[64:65], s[50:51], s44, v64, 0
	v_mad_i64_i32 v[66:67], s[50:51], s44, v66, 0
	v_cvt_pk_fp8_f32 v37, v32, v33
	v_lshl_add_u64 v[64:65], v[64:65], 2, s[46:47]
	v_lshl_add_u64 v[66:67], v[66:67], 2, s[46:47]
	v_lshl_add_u64 v[64:65], v[64:65], 0, s[48:49]
	v_lshl_add_u64 v[66:67], v[66:67], 0, s[48:49]
	v_mul_f32_e32 v36, 0x42800000, v38
	v_mul_f32_e32 v33, 0x42800000, v34
	v_lshl_add_u64 v[64:65], v[64:65], 0, v[128:129]
	v_lshl_add_u64 v[66:67], v[66:67], 0, v[128:129]
	v_med3_f32 v32, v36, s58, v153
	v_med3_f32 v33, v33, s58, v153
	global_load_dwordx4 v[108:111], v[64:65], off nt
	global_load_dwordx4 v[104:107], v[66:67], off nt
	v_or_b32_e32 v64, s28, v140
	v_or_b32_e32 v66, s28, v141
	v_cvt_pk_fp8_f32 v37, v32, v33 op_sel:[0,0,1]
	v_mul_f32_e32 v32, 0x42800000, v47
	v_mul_f32_e32 v33, 0x42800000, v43
	v_mad_i64_i32 v[64:65], s[50:51], s44, v64, 0
	v_mad_i64_i32 v[66:67], s[50:51], s44, v66, 0
	v_med3_f32 v32, v32, s58, v153
	v_med3_f32 v33, v33, s58, v153
	v_mov_b32_e32 v36, v129
	v_lshl_add_u64 v[64:65], v[64:65], 2, s[46:47]
	v_lshl_add_u64 v[66:67], v[66:67], 2, s[46:47]
	v_cvt_pk_fp8_f32 v36, v32, v33
	v_lshl_add_u64 v[64:65], v[64:65], 0, s[48:49]
	v_lshl_add_u64 v[66:67], v[66:67], 0, s[48:49]
	v_lshl_add_u64 v[64:65], v[64:65], 0, v[128:129]
	v_lshl_add_u64 v[66:67], v[66:67], 0, v[128:129]
	v_mul_f32_e32 v34, 0x42800000, v39
	v_mul_f32_e32 v33, 0x42800000, v35
	global_load_dwordx4 v[84:87], v[64:65], off nt
	global_load_dwordx4 v[80:83], v[66:67], off nt
	v_or_b32_e32 v64, s28, v142
	v_or_b32_e32 v66, s28, v143
	v_med3_f32 v32, v34, s58, v153
	v_med3_f32 v33, v33, s58, v153
	v_mul_f32_e32 v28, 0x42800000, v28
	v_mul_f32_e32 v24, 0x42800000, v24
	v_mad_i64_i32 v[64:65], s[50:51], s44, v64, 0
	v_mad_i64_i32 v[66:67], s[50:51], s44, v66, 0
	v_cvt_pk_fp8_f32 v36, v32, v33 op_sel:[0,0,1]
	v_med3_f32 v28, v28, s58, v153
	v_med3_f32 v24, v24, s58, v153
	v_mov_b32_e32 v32, v129
	v_lshl_add_u64 v[64:65], v[64:65], 2, s[46:47]
	v_lshl_add_u64 v[66:67], v[66:67], 2, s[46:47]
	v_cvt_pk_fp8_f32 v32, v28, v24
	v_lshl_add_u64 v[64:65], v[64:65], 0, s[48:49]
	v_lshl_add_u64 v[66:67], v[66:67], 0, s[48:49]
	v_lshl_add_u64 v[64:65], v[64:65], 0, v[128:129]
	v_lshl_add_u64 v[66:67], v[66:67], 0, v[128:129]
	v_mul_f32_e32 v20, 0x42800000, v20
	v_mul_f32_e32 v16, 0x42800000, v16
	global_load_dwordx4 v[92:95], v[64:65], off nt
	global_load_dwordx4 v[88:91], v[66:67], off nt
	v_or_b32_e32 v64, s28, v144
	v_or_b32_e32 v66, s28, v145
	v_or_b32_e32 v72, s28, v146
	v_or_b32_e32 v74, s28, v147
	v_med3_f32 v20, v20, s58, v153
	v_med3_f32 v16, v16, s58, v153
	v_mad_i64_i32 v[64:65], s[50:51], s44, v64, 0
	v_mad_i64_i32 v[66:67], s[50:51], s44, v66, 0
	v_mad_i64_i32 v[72:73], s[50:51], s44, v72, 0
	v_mad_i64_i32 v[74:75], s[44:45], s44, v74, 0
	v_cvt_pk_fp8_f32 v32, v20, v16 op_sel:[0,0,1]
	v_mul_f32_e32 v16, 0x42800000, v29
	v_mul_f32_e32 v20, 0x42800000, v25
	v_lshl_add_u64 v[64:65], v[64:65], 2, s[46:47]
	v_lshl_add_u64 v[66:67], v[66:67], 2, s[46:47]
	v_lshl_add_u64 v[72:73], v[72:73], 2, s[46:47]
	v_lshl_add_u64 v[74:75], v[74:75], 2, s[46:47]
	v_med3_f32 v16, v16, s58, v153
	v_med3_f32 v20, v20, s58, v153
	v_mov_b32_e32 v24, v129
	v_lshl_add_u64 v[64:65], v[64:65], 0, s[48:49]
	v_lshl_add_u64 v[66:67], v[66:67], 0, s[48:49]
	v_lshl_add_u64 v[72:73], v[72:73], 0, s[48:49]
	v_lshl_add_u64 v[74:75], v[74:75], 0, s[48:49]
	v_cvt_pk_fp8_f32 v24, v16, v20
	v_lshl_add_u64 v[64:65], v[64:65], 0, v[128:129]
	v_lshl_add_u64 v[66:67], v[66:67], 0, v[128:129]
	v_lshl_add_u64 v[72:73], v[72:73], 0, v[128:129]
	v_lshl_add_u64 v[74:75], v[74:75], 0, v[128:129]
	global_load_dwordx4 v[68:71], v[64:65], off nt
	s_nop 0
	global_load_dwordx4 v[64:67], v[66:67], off nt
	s_nop 0
	global_load_dwordx4 v[76:79], v[72:73], off nt
	s_nop 0
	global_load_dwordx4 v[72:75], v[74:75], off nt
	v_mul_f32_e32 v21, 0x42800000, v21
	v_mul_f32_e32 v17, 0x42800000, v17
	v_med3_f32 v16, v21, s58, v153
	v_med3_f32 v17, v17, s58, v153
	v_cvt_pk_fp8_f32 v24, v16, v17 op_sel:[0,0,1]
	v_mul_f32_e32 v16, 0x42800000, v30
	v_mul_f32_e32 v17, 0x42800000, v26
	v_med3_f32 v16, v16, s58, v153
	v_med3_f32 v17, v17, s58, v153
	v_mov_b32_e32 v21, v129
	v_cvt_pk_fp8_f32 v21, v16, v17
	v_mul_f32_e32 v20, 0x42800000, v22
	v_mul_f32_e32 v17, 0x42800000, v18
	v_med3_f32 v16, v20, s58, v153
	v_med3_f32 v17, v17, s58, v153
	v_cvt_pk_fp8_f32 v21, v16, v17 op_sel:[0,0,1]
	v_mul_f32_e32 v16, 0x42800000, v31
	v_mul_f32_e32 v17, 0x42800000, v27
	v_med3_f32 v16, v16, s58, v153
	v_med3_f32 v17, v17, s58, v153
	v_mov_b32_e32 v20, v129
	v_cvt_pk_fp8_f32 v20, v16, v17
	v_mul_f32_e32 v18, 0x42800000, v23
	v_mul_f32_e32 v17, 0x42800000, v19
	v_med3_f32 v16, v18, s58, v153
	v_med3_f32 v17, v17, s58, v153
	v_mul_f32_e32 v12, 0x42800000, v12
	v_mul_f32_e32 v8, 0x42800000, v8
	v_cvt_pk_fp8_f32 v20, v16, v17 op_sel:[0,0,1]
	v_med3_f32 v12, v12, s58, v153
	v_med3_f32 v8, v8, s58, v153
	v_mov_b32_e32 v16, v129
	v_cvt_pk_fp8_f32 v16, v12, v8
	v_mul_f32_e32 v4, 0x42800000, v4
	v_mul_f32_e32 v0, 0x42800000, v0
	v_med3_f32 v4, v4, s58, v153
	v_med3_f32 v0, v0, s58, v153
	v_cvt_pk_fp8_f32 v16, v4, v0 op_sel:[0,0,1]
	v_mul_f32_e32 v0, 0x42800000, v13
	v_mul_f32_e32 v4, 0x42800000, v9
	v_med3_f32 v0, v0, s58, v153
	v_med3_f32 v4, v4, s58, v153
	v_mov_b32_e32 v8, v129
	v_cvt_pk_fp8_f32 v8, v0, v4
	v_mul_f32_e32 v5, 0x42800000, v5
	v_mul_f32_e32 v1, 0x42800000, v1
	v_med3_f32 v0, v5, s58, v153
	v_med3_f32 v1, v1, s58, v153
	v_cvt_pk_fp8_f32 v8, v0, v1 op_sel:[0,0,1]
	v_mul_f32_e32 v0, 0x42800000, v14
	v_mul_f32_e32 v1, 0x42800000, v10
	v_med3_f32 v0, v0, s58, v153
	v_med3_f32 v1, v1, s58, v153
	v_mov_b32_e32 v5, v129
	v_cvt_pk_fp8_f32 v5, v0, v1
	v_mul_f32_e32 v4, 0x42800000, v6
	v_mul_f32_e32 v1, 0x42800000, v2
	v_med3_f32 v0, v4, s58, v153
	v_med3_f32 v1, v1, s58, v153
	v_cvt_pk_fp8_f32 v5, v0, v1 op_sel:[0,0,1]
	v_mul_f32_e32 v0, 0x42800000, v15
	v_mul_f32_e32 v1, 0x42800000, v11
	v_med3_f32 v0, v0, s58, v153
	v_med3_f32 v1, v1, s58, v153
	v_mov_b32_e32 v4, v129
	v_cvt_pk_fp8_f32 v4, v0, v1
	v_mul_f32_e32 v2, 0x42800000, v7
	v_mul_f32_e32 v1, 0x42800000, v3
	v_med3_f32 v0, v2, s58, v153
	v_med3_f32 v1, v1, s58, v153
	s_ashr_i32 s17, s20, 7
	v_cvt_pk_fp8_f32 v4, v0, v1 op_sel:[0,0,1]
	s_ashr_i32 s18, s17, 31
	s_and_b32 s20, s20, 0x60
	ds_write2_b32 v149, v155, v48 offset1:8
	ds_write2_b32 v149, v56, v40 offset0:34 offset1:42
	ds_write2_b32 v149, v53, v37 offset0:68 offset1:76
	ds_write2_b32 v149, v52, v36 offset0:102 offset1:110
	ds_write2_b32 v149, v32, v16 offset0:16 offset1:24
	ds_write2_b32 v149, v24, v8 offset0:50 offset1:58
	ds_write2_b32 v149, v21, v5 offset0:84 offset1:92
	ds_write2_b32 v149, v20, v4 offset0:118 offset1:126
	v_or_b32_e32 v4, s20, v148
	v_mov_b32_e32 v5, v129
	v_mov_b32_e32 v12, s17
	s_mul_i32 s18, s12, s18
	s_mul_i32 s13, s13, s17
	s_waitcnt lgkmcnt(0)
	v_mad_u64_u32 v[4:5], s[44:45], s12, v12, v[4:5]
	s_add_i32 s18, s18, s13
	ds_read2_b64 v[0:3], v154 offset1:1
	v_add_u32_e32 v5, s18, v5
	v_mov_b64_e32 v[8:9], s[42:43]
	v_mul_lo_u32 v6, v5, s14
	v_mul_lo_u32 v7, v4, s15
	v_mad_u64_u32 v[4:5], s[42:43], v4, s14, v[8:9]
	v_add3_u32 v5, v6, v5, v7
	s_ashr_i32 s17, s16, 31
	v_lshl_add_u64 v[4:5], v[4:5], 0, s[16:17]
	v_lshl_add_u64 v[10:11], v[4:5], 0, v[130:131]
	ds_read2_b64 v[4:7], v154 offset0:136 offset1:137
	s_waitcnt lgkmcnt(1)
	global_store_dwordx4 v[10:11], v[0:3], off sc1 nt
	v_add_u32_e32 v155, 0x880, v154
	v_add_u32_e32 v156, 0xcc0, v154
	v_or_b32_e32 v0, s20, v150
	v_mov_b32_e32 v1, v129
	v_mad_u64_u32 v[0:1], s[42:43], s12, v12, v[0:1]
	v_add_u32_e32 v1, s18, v1
	v_mul_lo_u32 v2, v1, s14
	v_mul_lo_u32 v3, v0, s15
	v_mad_u64_u32 v[0:1], s[42:43], v0, s14, v[8:9]
	v_add3_u32 v1, v2, v1, v3
	v_lshl_add_u64 v[0:1], v[0:1], 0, s[16:17]
	v_lshl_add_u64 v[0:1], v[0:1], 0, v[130:131]
	s_waitcnt lgkmcnt(0)
	global_store_dwordx4 v[0:1], v[4:7], off sc1 nt
	ds_read2_b64 v[0:3], v155 offset1:1
	s_nop 0
	v_or_b32_e32 v4, s20, v151
	v_mov_b32_e32 v5, v129
	v_mad_u64_u32 v[4:5], s[42:43], s12, v12, v[4:5]
	v_add_u32_e32 v5, s18, v5
	v_mul_lo_u32 v6, v5, s14
	v_mul_lo_u32 v7, v4, s15
	v_mad_u64_u32 v[4:5], s[42:43], v4, s14, v[8:9]
	v_add3_u32 v5, v6, v5, v7
	v_lshl_add_u64 v[4:5], v[4:5], 0, s[16:17]
	v_lshl_add_u64 v[10:11], v[4:5], 0, v[130:131]
	ds_read2_b64 v[4:7], v156 offset1:1
	s_waitcnt lgkmcnt(1)
	global_store_dwordx4 v[10:11], v[0:3], off sc1 nt
	s_nop 1
	v_or_b32_e32 v0, s20, v152
	v_mov_b32_e32 v1, v129
	v_mad_u64_u32 v[0:1], s[12:13], s12, v12, v[0:1]
	v_add_u32_e32 v1, s18, v1
	v_mul_lo_u32 v2, v1, s14
	v_mul_lo_u32 v3, v0, s15
	v_mad_u64_u32 v[0:1], s[12:13], v0, s14, v[8:9]
	s_add_i32 s12, s56, s55
	s_cmp_lt_i32 s12, s53
	s_cselect_b32 s29, s12, s21
	s_mul_hi_i32 s12, s29, 0x3e0f83e1
	s_lshr_b32 s13, s12, 31
	s_ashr_i32 s18, s12, 9
	s_add_i32 s18, s18, s13
	v_add3_u32 v1, v2, v1, v3
	s_mul_i32 s12, s18, 0xfffff7c0
	v_lshl_add_u64 v[0:1], v[0:1], 0, s[16:17]
	s_add_i32 s16, s12, s29
	s_add_i32 s12, s16, 0xfffffd40
	s_cmpk_lt_u32 s12, 0x2c0
	s_cselect_b64 s[12:13], -1, 0
	s_and_b64 s[14:15], s[12:13], exec
	v_lshl_add_u64 v[0:1], v[0:1], 0, v[130:131]
	s_cselect_b32 s17, 0xfffffd40, 0
	s_cmpk_lt_i32 s16, 0x580
	s_waitcnt lgkmcnt(0)
	global_store_dwordx4 v[0:1], v[4:7], off sc1 nt
	s_cselect_b64 s[14:15], -1, 0
	s_waitcnt lgkmcnt(0)
	s_and_b64 vcc, s[14:15], exec
	s_cselect_b32 s23, s17, 0xfffffa80
	s_add_i32 s23, s23, s16
	s_mov_b64 s[16:17], -1
	s_cbranch_vccnz .LBB0_287
	s_and_b32 s20, s29, 31
	s_ashr_i32 s21, s23, 5
	s_mov_b64 s[48:49], s[8:9]
	s_cbranch_execz .LBB0_288

.LBB0_290:
	s_lshl_b32 s20, s20, 5
	s_lshl_b32 s16, s21, 7
	s_lshl_b64 s[50:51], s[50:51], 2
	s_add_u32 s48, s48, s50
	v_or_b32_e32 v0, s16, v132
	v_or_b32_e32 v2, s16, v133
	s_addc_u32 s49, s49, s51
	v_mad_i64_i32 v[0:1], s[50:51], s46, v0, 0
	s_ashr_i32 s21, s20, 31
	v_mad_i64_i32 v[2:3], s[60:61], s46, v2, 0
	v_lshl_add_u64 v[0:1], v[0:1], 2, s[48:49]
	s_lshl_b64 s[50:51], s[20:21], 2
	v_lshl_add_u64 v[2:3], v[2:3], 2, s[48:49]
	v_lshl_add_u64 v[0:1], v[0:1], 0, s[50:51]
	v_lshl_add_u64 v[2:3], v[2:3], 0, s[50:51]
	v_lshl_add_u64 v[0:1], v[0:1], 0, v[128:129]
	v_lshl_add_u64 v[2:3], v[2:3], 0, v[128:129]
	global_load_dwordx4 v[60:63], v[0:1], off nt
	global_load_dwordx4 v[56:59], v[2:3], off nt
	v_or_b32_e32 v0, s16, v134
	v_or_b32_e32 v2, s16, v135
	v_mad_i64_i32 v[0:1], s[60:61], s46, v0, 0
	v_mad_i64_i32 v[2:3], s[60:61], s46, v2, 0
	v_lshl_add_u64 v[0:1], v[0:1], 2, s[48:49]
	v_lshl_add_u64 v[2:3], v[2:3], 2, s[48:49]
	v_lshl_add_u64 v[0:1], v[0:1], 0, s[50:51]
	v_lshl_add_u64 v[2:3], v[2:3], 0, s[50:51]
	v_lshl_add_u64 v[0:1], v[0:1], 0, v[128:129]
	v_lshl_add_u64 v[2:3], v[2:3], 0, v[128:129]
	global_load_dwordx4 v[52:55], v[0:1], off nt
	global_load_dwordx4 v[48:51], v[2:3], off nt
	v_or_b32_e32 v0, s16, v136
	v_or_b32_e32 v2, s16, v137
	v_mad_i64_i32 v[0:1], s[60:61], s46, v0, 0
	v_mad_i64_i32 v[2:3], s[60:61], s46, v2, 0
	v_lshl_add_u64 v[0:1], v[0:1], 2, s[48:49]
	v_lshl_add_u64 v[2:3], v[2:3], 2, s[48:49]
	v_lshl_add_u64 v[0:1], v[0:1], 0, s[50:51]
	v_lshl_add_u64 v[2:3], v[2:3], 0, s[50:51]
	v_lshl_add_u64 v[0:1], v[0:1], 0, v[128:129]
	v_lshl_add_u64 v[2:3], v[2:3], 0, v[128:129]
	global_load_dwordx4 v[44:47], v[0:1], off nt
	global_load_dwordx4 v[40:43], v[2:3], off nt
	v_or_b32_e32 v0, s16, v138
	v_or_b32_e32 v2, s16, v139
	v_mad_i64_i32 v[0:1], s[60:61], s46, v0, 0
	v_mad_i64_i32 v[2:3], s[60:61], s46, v2, 0
	v_lshl_add_u64 v[0:1], v[0:1], 2, s[48:49]
	v_lshl_add_u64 v[2:3], v[2:3], 2, s[48:49]
	v_lshl_add_u64 v[0:1], v[0:1], 0, s[50:51]
	v_lshl_add_u64 v[2:3], v[2:3], 0, s[50:51]
	v_lshl_add_u64 v[0:1], v[0:1], 0, v[128:129]
	v_lshl_add_u64 v[2:3], v[2:3], 0, v[128:129]
	global_load_dwordx4 v[36:39], v[0:1], off nt
	global_load_dwordx4 v[32:35], v[2:3], off nt
	v_or_b32_e32 v0, s16, v140
	v_or_b32_e32 v2, s16, v141
	v_mad_i64_i32 v[0:1], s[60:61], s46, v0, 0
	v_mad_i64_i32 v[2:3], s[60:61], s46, v2, 0
	v_lshl_add_u64 v[0:1], v[0:1], 2, s[48:49]
	v_lshl_add_u64 v[2:3], v[2:3], 2, s[48:49]
	v_lshl_add_u64 v[0:1], v[0:1], 0, s[50:51]
	v_lshl_add_u64 v[2:3], v[2:3], 0, s[50:51]
	v_lshl_add_u64 v[0:1], v[0:1], 0, v[128:129]
	v_lshl_add_u64 v[2:3], v[2:3], 0, v[128:129]
	global_load_dwordx4 v[28:31], v[0:1], off nt
	global_load_dwordx4 v[24:27], v[2:3], off nt
	v_or_b32_e32 v0, s16, v142
	v_or_b32_e32 v2, s16, v143
	v_mad_i64_i32 v[0:1], s[60:61], s46, v0, 0
	v_mad_i64_i32 v[2:3], s[60:61], s46, v2, 0
	v_lshl_add_u64 v[0:1], v[0:1], 2, s[48:49]
	v_lshl_add_u64 v[2:3], v[2:3], 2, s[48:49]
	v_lshl_add_u64 v[0:1], v[0:1], 0, s[50:51]
	v_lshl_add_u64 v[2:3], v[2:3], 0, s[50:51]
	v_lshl_add_u64 v[0:1], v[0:1], 0, v[128:129]
	v_lshl_add_u64 v[2:3], v[2:3], 0, v[128:129]
	global_load_dwordx4 v[20:23], v[0:1], off nt
	global_load_dwordx4 v[16:19], v[2:3], off nt
	v_or_b32_e32 v0, s16, v144
	v_or_b32_e32 v2, s16, v145
	v_mad_i64_i32 v[0:1], s[60:61], s46, v0, 0
	v_mad_i64_i32 v[2:3], s[60:61], s46, v2, 0
	v_lshl_add_u64 v[0:1], v[0:1], 2, s[48:49]
	v_lshl_add_u64 v[2:3], v[2:3], 2, s[48:49]
	v_lshl_add_u64 v[0:1], v[0:1], 0, s[50:51]
	v_lshl_add_u64 v[2:3], v[2:3], 0, s[50:51]
	v_lshl_add_u64 v[0:1], v[0:1], 0, v[128:129]
	v_lshl_add_u64 v[2:3], v[2:3], 0, v[128:129]
	global_load_dwordx4 v[12:15], v[0:1], off nt
	global_load_dwordx4 v[8:11], v[2:3], off nt
	v_or_b32_e32 v0, s16, v146
	v_or_b32_e32 v2, s16, v147
	v_mad_i64_i32 v[0:1], s[60:61], s46, v0, 0
	v_mad_i64_i32 v[2:3], s[46:47], s46, v2, 0
	v_lshl_add_u64 v[0:1], v[0:1], 2, s[48:49]
	v_lshl_add_u64 v[2:3], v[2:3], 2, s[48:49]
	v_lshl_add_u64 v[0:1], v[0:1], 0, s[50:51]
	v_lshl_add_u64 v[2:3], v[2:3], 0, s[50:51]
	v_lshl_add_u64 v[0:1], v[0:1], 0, v[128:129]
	v_lshl_add_u64 v[2:3], v[2:3], 0, v[128:129]
	global_load_dwordx4 v[4:7], v[0:1], off nt
	s_nop 0
	global_load_dwordx4 v[0:3], v[2:3], off nt
	s_andn2_b64 vcc, exec, s[36:37]
	s_cbranch_vccnz .LBB0_275
	s_waitcnt vmcnt(35)
	v_mul_f32_e32 v116, 0x42800000, v116
	s_waitcnt vmcnt(34)
	v_mul_f32_e32 v112, 0x42800000, v112
	v_med3_f32 v116, v116, s58, v153
	v_med3_f32 v112, v112, s58, v153
	v_mov_b32_e32 v157, v129
	v_cvt_pk_fp8_f32 v157, v116, v112
	s_waitcnt vmcnt(33)
	v_mul_f32_e32 v124, 0x42800000, v124
	s_waitcnt vmcnt(32)
	v_mul_f32_e32 v116, 0x42800000, v120
	v_med3_f32 v112, v124, s58, v153
	v_med3_f32 v116, v116, s58, v153
	v_cvt_pk_fp8_f32 v157, v112, v116 op_sel:[0,0,1]
	v_mul_f32_e32 v112, 0x42800000, v117
	v_mul_f32_e32 v113, 0x42800000, v113
	v_med3_f32 v112, v112, s58, v153
	v_med3_f32 v113, v113, s58, v153
	v_mov_b32_e32 v117, v129
	v_cvt_pk_fp8_f32 v117, v112, v113
	v_mul_f32_e32 v116, 0x42800000, v125
	v_mul_f32_e32 v113, 0x42800000, v121
	v_med3_f32 v112, v116, s58, v153
	v_med3_f32 v113, v113, s58, v153
	v_cvt_pk_fp8_f32 v117, v112, v113 op_sel:[0,0,1]
	v_mul_f32_e32 v112, 0x42800000, v118
	v_mul_f32_e32 v113, 0x42800000, v114
	v_med3_f32 v112, v112, s58, v153
	v_med3_f32 v113, v113, s58, v153
	v_mov_b32_e32 v116, v129
	v_cvt_pk_fp8_f32 v116, v112, v113
	v_mul_f32_e32 v114, 0x42800000, v126
	v_mul_f32_e32 v113, 0x42800000, v122
	v_med3_f32 v112, v114, s58, v153
	v_med3_f32 v113, v113, s58, v153
	v_cvt_pk_fp8_f32 v116, v112, v113 op_sel:[0,0,1]
	v_mul_f32_e32 v112, 0x42800000, v119
	v_mul_f32_e32 v113, 0x42800000, v115
	v_med3_f32 v112, v112, s58, v153
	v_med3_f32 v113, v113, s58, v153
	v_mov_b32_e32 v115, v129
	v_cvt_pk_fp8_f32 v115, v112, v113
	v_mul_f32_e32 v114, 0x42800000, v127
	v_mul_f32_e32 v113, 0x42800000, v123
	v_med3_f32 v112, v114, s58, v153
	v_med3_f32 v113, v113, s58, v153
	s_waitcnt vmcnt(31)
	v_mul_f32_e32 v100, 0x42800000, v100
	s_waitcnt vmcnt(30)
	v_mul_f32_e32 v96, 0x42800000, v96
	v_cvt_pk_fp8_f32 v115, v112, v113 op_sel:[0,0,1]
	v_med3_f32 v100, v100, s58, v153
	v_med3_f32 v96, v96, s58, v153
	v_mov_b32_e32 v112, v129
	v_cvt_pk_fp8_f32 v112, v100, v96
	s_waitcnt vmcnt(29)
	v_mul_f32_e32 v108, 0x42800000, v108
	s_waitcnt vmcnt(28)
	v_mul_f32_e32 v100, 0x42800000, v104
	v_med3_f32 v96, v108, s58, v153
	v_med3_f32 v100, v100, s58, v153
	v_cvt_pk_fp8_f32 v112, v96, v100 op_sel:[0,0,1]
	v_mul_f32_e32 v96, 0x42800000, v101
	v_mul_f32_e32 v97, 0x42800000, v97
	v_med3_f32 v96, v96, s58, v153
	v_med3_f32 v97, v97, s58, v153
	v_mov_b32_e32 v101, v129
	v_cvt_pk_fp8_f32 v101, v96, v97
	v_mul_f32_e32 v100, 0x42800000, v109
	v_mul_f32_e32 v97, 0x42800000, v105
	v_med3_f32 v96, v100, s58, v153
	v_med3_f32 v97, v97, s58, v153
	v_cvt_pk_fp8_f32 v101, v96, v97 op_sel:[0,0,1]
	v_mul_f32_e32 v96, 0x42800000, v102
	v_mul_f32_e32 v97, 0x42800000, v98
	v_med3_f32 v96, v96, s58, v153
	v_med3_f32 v97, v97, s58, v153
	v_mov_b32_e32 v100, v129
	v_cvt_pk_fp8_f32 v100, v96, v97
	v_mul_f32_e32 v98, 0x42800000, v110
	v_mul_f32_e32 v97, 0x42800000, v106
	v_med3_f32 v96, v98, s58, v153
	v_med3_f32 v97, v97, s58, v153
	v_cvt_pk_fp8_f32 v100, v96, v97 op_sel:[0,0,1]
	v_mul_f32_e32 v96, 0x42800000, v103
	v_mul_f32_e32 v97, 0x42800000, v99
	v_med3_f32 v96, v96, s58, v153
	v_med3_f32 v97, v97, s58, v153
	v_mov_b32_e32 v99, v129
	v_cvt_pk_fp8_f32 v99, v96, v97
	v_mul_f32_e32 v98, 0x42800000, v111
	v_mul_f32_e32 v97, 0x42800000, v107
	v_med3_f32 v96, v98, s58, v153
	v_med3_f32 v97, v97, s58, v153
	s_waitcnt vmcnt(27)
	v_mul_f32_e32 v84, 0x42800000, v84
	s_waitcnt vmcnt(26)
	v_mul_f32_e32 v80, 0x42800000, v80
	v_cvt_pk_fp8_f32 v99, v96, v97 op_sel:[0,0,1]
	v_med3_f32 v84, v84, s58, v153
	v_med3_f32 v80, v80, s58, v153
	v_mov_b32_e32 v96, v129
	v_cvt_pk_fp8_f32 v96, v84, v80
	s_waitcnt vmcnt(25)
	v_mul_f32_e32 v92, 0x42800000, v92
	s_waitcnt vmcnt(24)
	v_mul_f32_e32 v84, 0x42800000, v88
	v_med3_f32 v80, v92, s58, v153
	v_med3_f32 v84, v84, s58, v153
	v_cvt_pk_fp8_f32 v96, v80, v84 op_sel:[0,0,1]
	v_mul_f32_e32 v80, 0x42800000, v85
	v_mul_f32_e32 v81, 0x42800000, v81
	v_med3_f32 v80, v80, s58, v153
	v_med3_f32 v81, v81, s58, v153
	v_mov_b32_e32 v85, v129
	v_cvt_pk_fp8_f32 v85, v80, v81
	v_mul_f32_e32 v84, 0x42800000, v93
	v_mul_f32_e32 v81, 0x42800000, v89
	v_med3_f32 v80, v84, s58, v153
	v_med3_f32 v81, v81, s58, v153
	v_cvt_pk_fp8_f32 v85, v80, v81 op_sel:[0,0,1]
	v_mul_f32_e32 v80, 0x42800000, v86
	v_mul_f32_e32 v81, 0x42800000, v82
	v_med3_f32 v80, v80, s58, v153
	v_med3_f32 v81, v81, s58, v153
	v_mov_b32_e32 v84, v129
	v_cvt_pk_fp8_f32 v84, v80, v81
	v_mul_f32_e32 v82, 0x42800000, v94
	v_mul_f32_e32 v81, 0x42800000, v90
	v_med3_f32 v80, v82, s58, v153
	v_med3_f32 v81, v81, s58, v153
	v_cvt_pk_fp8_f32 v84, v80, v81 op_sel:[0,0,1]
	v_mul_f32_e32 v80, 0x42800000, v87
	v_mul_f32_e32 v81, 0x42800000, v83
	v_med3_f32 v80, v80, s58, v153
	v_med3_f32 v81, v81, s58, v153
	v_mov_b32_e32 v83, v129
	v_cvt_pk_fp8_f32 v83, v80, v81
	v_mul_f32_e32 v82, 0x42800000, v95
	v_mul_f32_e32 v81, 0x42800000, v91
	v_med3_f32 v80, v82, s58, v153
	v_med3_f32 v81, v81, s58, v153
	s_waitcnt vmcnt(23)
	v_mul_f32_e32 v68, 0x42800000, v68
	s_waitcnt vmcnt(22)
	v_mul_f32_e32 v64, 0x42800000, v64
	v_cvt_pk_fp8_f32 v83, v80, v81 op_sel:[0,0,1]
	v_med3_f32 v68, v68, s58, v153
	v_med3_f32 v64, v64, s58, v153
	v_mov_b32_e32 v80, v129
	v_cvt_pk_fp8_f32 v80, v68, v64
	s_waitcnt vmcnt(21)
	v_mul_f32_e32 v76, 0x42800000, v76
	s_waitcnt vmcnt(20)
	v_mul_f32_e32 v68, 0x42800000, v72
	v_med3_f32 v64, v76, s58, v153
	v_med3_f32 v68, v68, s58, v153
	v_cvt_pk_fp8_f32 v80, v64, v68 op_sel:[0,0,1]
	v_mul_f32_e32 v64, 0x42800000, v69
	v_mul_f32_e32 v65, 0x42800000, v65
	v_med3_f32 v64, v64, s58, v153
	v_med3_f32 v65, v65, s58, v153
	v_mov_b32_e32 v69, v129
	v_cvt_pk_fp8_f32 v69, v64, v65
	v_mul_f32_e32 v68, 0x42800000, v77
	v_mul_f32_e32 v65, 0x42800000, v73
	v_med3_f32 v64, v68, s58, v153
	v_med3_f32 v65, v65, s58, v153
	v_cvt_pk_fp8_f32 v69, v64, v65 op_sel:[0,0,1]
	v_mul_f32_e32 v64, 0x42800000, v70
	v_mul_f32_e32 v65, 0x42800000, v66
	v_med3_f32 v64, v64, s58, v153
	v_med3_f32 v65, v65, s58, v153
	v_mov_b32_e32 v68, v129
	v_cvt_pk_fp8_f32 v68, v64, v65
	v_mul_f32_e32 v66, 0x42800000, v78
	v_mul_f32_e32 v65, 0x42800000, v74
	v_med3_f32 v64, v66, s58, v153
	v_med3_f32 v65, v65, s58, v153
	v_cvt_pk_fp8_f32 v68, v64, v65 op_sel:[0,0,1]
	v_mul_f32_e32 v64, 0x42800000, v71
	v_mul_f32_e32 v65, 0x42800000, v67
	v_med3_f32 v64, v64, s58, v153
	v_med3_f32 v65, v65, s58, v153
	v_mov_b32_e32 v67, v129
	v_cvt_pk_fp8_f32 v67, v64, v65
	s_add_u32 s17, s10, s38
	v_mul_f32_e32 v66, 0x42800000, v79
	v_mul_f32_e32 v65, 0x42800000, v75
	s_addc_u32 s18, s11, s39
	v_med3_f32 v64, v66, s58, v153
	v_med3_f32 v65, v65, s58, v153
	s_add_u32 s36, s17, s40
	v_cvt_pk_fp8_f32 v67, v64, v65 op_sel:[0,0,1]
	s_addc_u32 s37, s18, s41
	ds_write2_b32 v149, v157, v112 offset1:8
	ds_write2_b32 v149, v117, v101 offset0:34 offset1:42
	ds_write2_b32 v149, v116, v100 offset0:68 offset1:76
	ds_write2_b32 v149, v115, v99 offset0:102 offset1:110
	ds_write2_b32 v149, v96, v80 offset0:16 offset1:24
	ds_write2_b32 v149, v85, v69 offset0:50 offset1:58
	ds_write2_b32 v149, v84, v68 offset0:84 offset1:92
	ds_write2_b32 v149, v83, v67 offset0:118 offset1:126
	s_ashr_i32 s17, s59, 2
	s_and_b32 s21, s34, 0x60
	s_waitcnt lgkmcnt(0)
	s_mul_hi_i32 s18, s30, s17
	s_mul_i32 s17, s30, s17
	v_or_b32_e32 v68, s21, v148
	ds_read2_b64 v[64:67], v154 offset1:1
	v_or_b32_e32 v68, s17, v68
	v_mov_b64_e32 v[72:73], s[36:37]
	v_mad_u64_u32 v[68:69], s[30:31], v68, s22, v[72:73]
	v_mov_b32_e32 v76, s22
	v_mad_i32_i24 v69, s18, v76, v69
	s_ashr_i32 s29, s28, 31
	v_lshl_add_u64 v[68:69], v[68:69], 0, s[28:29]
	v_lshl_add_u64 v[74:75], v[68:69], 0, v[130:131]
	ds_read2_b64 v[68:71], v154 offset0:136 offset1:137
	s_waitcnt lgkmcnt(1)
	global_store_dwordx4 v[74:75], v[64:67], off sc1 nt
	s_nop 1
	v_or_b32_e32 v64, s21, v150
	v_or_b32_e32 v64, s17, v64
	v_mad_u64_u32 v[64:65], s[30:31], v64, s22, v[72:73]
	v_mad_i32_i24 v65, s18, v76, v65
	v_lshl_add_u64 v[64:65], v[64:65], 0, s[28:29]
	v_lshl_add_u64 v[64:65], v[64:65], 0, v[130:131]
	s_waitcnt lgkmcnt(0)
	global_store_dwordx4 v[64:65], v[68:71], off sc1 nt
	ds_read2_b64 v[64:67], v155 offset1:1
	s_nop 0
	v_or_b32_e32 v68, s21, v151
	v_or_b32_e32 v68, s17, v68
	v_mad_u64_u32 v[68:69], s[30:31], v68, s22, v[72:73]
	v_mad_i32_i24 v69, s18, v76, v69
	v_lshl_add_u64 v[68:69], v[68:69], 0, s[28:29]
	v_lshl_add_u64 v[74:75], v[68:69], 0, v[130:131]
	ds_read2_b64 v[68:71], v156 offset1:1
	s_waitcnt lgkmcnt(1)
	global_store_dwordx4 v[74:75], v[64:67], off sc1 nt
	s_nop 1
	v_or_b32_e32 v64, s21, v152
	v_or_b32_e32 v64, s17, v64
	v_mad_u64_u32 v[64:65], s[22:23], v64, s22, v[72:73]
	v_mad_i32_i24 v65, s18, v76, v65
	v_lshl_add_u64 v[64:65], v[64:65], 0, s[28:29]
	v_lshl_add_u64 v[64:65], v[64:65], 0, v[130:131]
	s_waitcnt lgkmcnt(0)
	global_store_dwordx4 v[64:65], v[68:71], off sc1 nt
	s_waitcnt lgkmcnt(0)
	s_branch .LBB0_275

.LBB0_716:
	s_waitcnt lgkmcnt(0)
	s_add_u32 s12, s10, s16
	s_addc_u32 s15, s11, s17
	s_lshl_b32 s20, s34, 5
	s_lshl_b32 s16, s21, 7
	s_lshl_b64 s[26:27], s[26:27], 2
	s_add_u32 s26, s22, s26
	s_addc_u32 s27, s23, s27
	s_add_u32 s22, s12, s28
	v_or_b32_e32 v23, s16, v13
	s_addc_u32 s23, s15, s29
	v_mad_i64_i32 v[0:1], s[28:29], s24, v23, 0
	s_ashr_i32 s21, s20, 31
	v_or_b32_e32 v2, 1, v23
	v_lshl_add_u64 v[0:1], v[0:1], 2, s[26:27]
	s_lshl_b64 s[28:29], s[20:21], 2
	v_mad_i64_i32 v[2:3], s[36:37], s24, v2, 0
	v_lshl_add_u64 v[0:1], v[0:1], 0, s[28:29]
	v_lshl_add_u64 v[2:3], v[2:3], 2, s[26:27]
	v_lshl_add_u64 v[0:1], v[0:1], 0, v[10:11]
	v_lshl_add_u64 v[2:3], v[2:3], 0, s[28:29]
	v_lshl_add_u64 v[2:3], v[2:3], 0, v[10:11]
	global_load_dwordx4 v[24:27], v[0:1], off nt
	global_load_dwordx4 v[28:31], v[2:3], off nt
	v_or_b32_e32 v0, 2, v23
	s_waitcnt vmcnt(14)
	v_or_b32_e32 v76, s16, v12
	v_mad_i64_i32 v[0:1], s[36:37], s24, v0, 0
	v_or_b32_e32 v2, 3, v76
	v_lshl_add_u64 v[0:1], v[0:1], 2, s[26:27]
	v_mad_i64_i32 v[2:3], s[36:37], s24, v2, 0
	v_lshl_add_u64 v[0:1], v[0:1], 0, s[28:29]
	v_lshl_add_u64 v[2:3], v[2:3], 2, s[26:27]
	v_lshl_add_u64 v[0:1], v[0:1], 0, v[10:11]
	v_lshl_add_u64 v[2:3], v[2:3], 0, s[28:29]
	v_lshl_add_u64 v[2:3], v[2:3], 0, v[10:11]
	global_load_dwordx4 v[32:35], v[0:1], off nt
	global_load_dwordx4 v[36:39], v[2:3], off nt
	v_or_b32_e32 v0, 32, v23
	v_mad_i64_i32 v[0:1], s[36:37], s24, v0, 0
	v_or_b32_e32 v2, 33, v23
	v_lshl_add_u64 v[0:1], v[0:1], 2, s[26:27]
	v_mad_i64_i32 v[2:3], s[36:37], s24, v2, 0
	v_lshl_add_u64 v[0:1], v[0:1], 0, s[28:29]
	v_lshl_add_u64 v[2:3], v[2:3], 2, s[26:27]
	v_lshl_add_u64 v[0:1], v[0:1], 0, v[10:11]
	v_lshl_add_u64 v[2:3], v[2:3], 0, s[28:29]
	v_lshl_add_u64 v[2:3], v[2:3], 0, v[10:11]
	global_load_dwordx4 v[40:43], v[0:1], off nt
	global_load_dwordx4 v[44:47], v[2:3], off nt
	v_or_b32_e32 v0, 34, v23
	v_mad_i64_i32 v[0:1], s[36:37], s24, v0, 0
	v_or_b32_e32 v2, 35, v76
	v_lshl_add_u64 v[0:1], v[0:1], 2, s[26:27]
	v_mad_i64_i32 v[2:3], s[36:37], s24, v2, 0
	v_lshl_add_u64 v[0:1], v[0:1], 0, s[28:29]
	v_lshl_add_u64 v[2:3], v[2:3], 2, s[26:27]
	v_lshl_add_u64 v[0:1], v[0:1], 0, v[10:11]
	v_lshl_add_u64 v[2:3], v[2:3], 0, s[28:29]
	v_lshl_add_u64 v[2:3], v[2:3], 0, v[10:11]
	global_load_dwordx4 v[48:51], v[0:1], off nt
	global_load_dwordx4 v[52:55], v[2:3], off nt
	v_or_b32_e32 v0, 64, v23
	v_mad_i64_i32 v[0:1], s[36:37], s24, v0, 0
	v_or_b32_e32 v2, 0x41, v23
	v_lshl_add_u64 v[0:1], v[0:1], 2, s[26:27]
	v_mad_i64_i32 v[2:3], s[36:37], s24, v2, 0
	v_lshl_add_u64 v[0:1], v[0:1], 0, s[28:29]
	v_lshl_add_u64 v[2:3], v[2:3], 2, s[26:27]
	v_lshl_add_u64 v[0:1], v[0:1], 0, v[10:11]
	v_lshl_add_u64 v[2:3], v[2:3], 0, s[28:29]
	v_lshl_add_u64 v[2:3], v[2:3], 0, v[10:11]
	global_load_dwordx4 v[56:59], v[0:1], off nt
	global_load_dwordx4 v[60:63], v[2:3], off nt
	v_or_b32_e32 v0, 0x42, v23
	v_mad_i64_i32 v[0:1], s[36:37], s24, v0, 0
	v_or_b32_e32 v2, 0x43, v76
	v_lshl_add_u64 v[0:1], v[0:1], 2, s[26:27]
	v_mad_i64_i32 v[2:3], s[36:37], s24, v2, 0
	v_lshl_add_u64 v[0:1], v[0:1], 0, s[28:29]
	v_lshl_add_u64 v[2:3], v[2:3], 2, s[26:27]
	v_lshl_add_u64 v[0:1], v[0:1], 0, v[10:11]
	v_lshl_add_u64 v[2:3], v[2:3], 0, s[28:29]
	v_lshl_add_u64 v[2:3], v[2:3], 0, v[10:11]
	global_load_dwordx4 v[64:67], v[0:1], off nt
	global_load_dwordx4 v[68:71], v[2:3], off nt
	v_or_b32_e32 v0, 0x60, v23
	v_mad_i64_i32 v[0:1], s[36:37], s24, v0, 0
	v_lshl_add_u64 v[0:1], v[0:1], 2, s[26:27]
	v_lshl_add_u64 v[0:1], v[0:1], 0, s[28:29]
	v_lshl_add_u64 v[72:73], v[0:1], 0, v[10:11]
	v_or_b32_e32 v0, 0x61, v23
	v_mad_i64_i32 v[0:1], s[36:37], s24, v0, 0
	v_lshl_add_u64 v[0:1], v[0:1], 2, s[26:27]
	v_lshl_add_u64 v[0:1], v[0:1], 0, s[28:29]
	v_or_b32_e32 v23, 0x62, v23
	v_lshl_add_u64 v[74:75], v[0:1], 0, v[10:11]
	global_load_dwordx4 v[4:7], v[72:73], off nt
	global_load_dwordx4 v[0:3], v[74:75], off nt
	v_mad_i64_i32 v[72:73], s[36:37], s24, v23, 0
	v_lshl_add_u64 v[72:73], v[72:73], 2, s[26:27]
	v_lshl_add_u64 v[72:73], v[72:73], 0, s[28:29]
	v_or_b32_e32 v23, 0x63, v76
	s_waitcnt vmcnt(25)
	v_lshl_add_u64 v[80:81], v[72:73], 0, v[10:11]
	v_mad_i64_i32 v[72:73], s[24:25], s24, v23, 0
	v_lshl_add_u64 v[72:73], v[72:73], 2, s[26:27]
	v_lshl_add_u64 v[72:73], v[72:73], 0, s[28:29]
	v_lshl_add_u64 v[82:83], v[72:73], 0, v[10:11]
	global_load_dwordx4 v[72:75], v[80:81], off nt
	global_load_dwordx4 v[76:79], v[82:83], off nt
	s_waitcnt vmcnt(15)
	v_mul_f32_e32 v23, 0x42800000, v24
	s_waitcnt vmcnt(14)
	v_mul_f32_e32 v24, 0x42800000, v28
	v_med3_f32 v23, v23, s33, v19
	v_med3_f32 v24, v24, s33, v19
	s_waitcnt vmcnt(13)
	v_mul_f32_e32 v28, 0x42800000, v32
	v_mov_b32_e32 v32, 0
	v_cvt_pk_fp8_f32 v32, v23, v24
	s_waitcnt vmcnt(12)
	v_mul_f32_e32 v24, 0x42800000, v36
	v_med3_f32 v23, v28, s33, v19
	v_med3_f32 v24, v24, s33, v19
	v_cvt_pk_fp8_f32 v32, v23, v24 op_sel:[0,0,1]
	v_mul_f32_e32 v23, 0x42800000, v25
	v_mul_f32_e32 v24, 0x42800000, v29
	v_med3_f32 v23, v23, s33, v19
	v_med3_f32 v24, v24, s33, v19
	v_mov_b32_e32 v28, 0
	v_cvt_pk_fp8_f32 v28, v23, v24
	v_mul_f32_e32 v25, 0x42800000, v33
	v_mul_f32_e32 v24, 0x42800000, v37
	v_med3_f32 v23, v25, s33, v19
	v_med3_f32 v24, v24, s33, v19
	v_cvt_pk_fp8_f32 v28, v23, v24 op_sel:[0,0,1]
	v_mul_f32_e32 v23, 0x42800000, v26
	v_mul_f32_e32 v24, 0x42800000, v30
	v_med3_f32 v23, v23, s33, v19
	v_med3_f32 v24, v24, s33, v19
	v_mov_b32_e32 v26, 0
	v_cvt_pk_fp8_f32 v26, v23, v24
	v_mul_f32_e32 v25, 0x42800000, v34
	v_mul_f32_e32 v24, 0x42800000, v38
	v_med3_f32 v23, v25, s33, v19
	v_med3_f32 v24, v24, s33, v19
	v_cvt_pk_fp8_f32 v26, v23, v24 op_sel:[0,0,1]
	v_mul_f32_e32 v23, 0x42800000, v27
	v_mul_f32_e32 v24, 0x42800000, v31
	v_med3_f32 v23, v23, s33, v19
	v_med3_f32 v24, v24, s33, v19
	v_mov_b32_e32 v27, 0
	v_cvt_pk_fp8_f32 v27, v23, v24
	v_mul_f32_e32 v25, 0x42800000, v35
	v_mul_f32_e32 v24, 0x42800000, v39
	v_med3_f32 v23, v25, s33, v19
	v_med3_f32 v24, v24, s33, v19
	v_cvt_pk_fp8_f32 v27, v23, v24 op_sel:[0,0,1]
	s_waitcnt vmcnt(11)
	v_mul_f32_e32 v23, 0x42800000, v40
	s_waitcnt vmcnt(10)
	v_mul_f32_e32 v24, 0x42800000, v44
	v_med3_f32 v23, v23, s33, v19
	v_med3_f32 v24, v24, s33, v19
	v_mov_b32_e32 v29, 0
	v_cvt_pk_fp8_f32 v29, v23, v24
	s_waitcnt vmcnt(9)
	v_mul_f32_e32 v25, 0x42800000, v48
	s_waitcnt vmcnt(8)
	v_mul_f32_e32 v24, 0x42800000, v52
	v_med3_f32 v23, v25, s33, v19
	v_med3_f32 v24, v24, s33, v19
	v_cvt_pk_fp8_f32 v29, v23, v24 op_sel:[0,0,1]
	v_mul_f32_e32 v23, 0x42800000, v41
	v_mul_f32_e32 v24, 0x42800000, v45
	v_med3_f32 v23, v23, s33, v19
	v_med3_f32 v24, v24, s33, v19
	v_mov_b32_e32 v30, 0
	v_cvt_pk_fp8_f32 v30, v23, v24
	v_mul_f32_e32 v25, 0x42800000, v49
	v_mul_f32_e32 v24, 0x42800000, v53
	v_med3_f32 v23, v25, s33, v19
	v_med3_f32 v24, v24, s33, v19
	v_cvt_pk_fp8_f32 v30, v23, v24 op_sel:[0,0,1]
	v_mul_f32_e32 v23, 0x42800000, v42
	v_mul_f32_e32 v24, 0x42800000, v46
	v_med3_f32 v23, v23, s33, v19
	v_med3_f32 v24, v24, s33, v19
	v_mov_b32_e32 v31, 0
	v_cvt_pk_fp8_f32 v31, v23, v24
	v_mul_f32_e32 v25, 0x42800000, v50
	v_mul_f32_e32 v24, 0x42800000, v54
	v_med3_f32 v23, v25, s33, v19
	v_med3_f32 v24, v24, s33, v19
	v_cvt_pk_fp8_f32 v31, v23, v24 op_sel:[0,0,1]
	v_mul_f32_e32 v23, 0x42800000, v43
	v_mul_f32_e32 v24, 0x42800000, v47
	v_med3_f32 v23, v23, s33, v19
	v_med3_f32 v24, v24, s33, v19
	v_mov_b32_e32 v33, 0
	v_cvt_pk_fp8_f32 v33, v23, v24
	v_mul_f32_e32 v25, 0x42800000, v51
	v_mul_f32_e32 v24, 0x42800000, v55
	v_med3_f32 v23, v25, s33, v19
	v_med3_f32 v24, v24, s33, v19
	v_cvt_pk_fp8_f32 v33, v23, v24 op_sel:[0,0,1]
	s_waitcnt vmcnt(7)
	v_mul_f32_e32 v23, 0x42800000, v56
	s_waitcnt vmcnt(6)
	v_mul_f32_e32 v24, 0x42800000, v60
	ds_write2_b32 v15, v32, v29 offset1:8
	ds_write2_b32 v15, v28, v30 offset0:34 offset1:42
	ds_write2_b32 v15, v26, v31 offset0:68 offset1:76
	ds_write2_b32 v15, v27, v33 offset0:102 offset1:110
	v_med3_f32 v23, v23, s33, v19
	v_med3_f32 v24, v24, s33, v19
	v_mov_b32_e32 v26, 0
	v_cvt_pk_fp8_f32 v26, v23, v24
	s_waitcnt vmcnt(5)
	v_mul_f32_e32 v25, 0x42800000, v64
	s_waitcnt vmcnt(4)
	v_mul_f32_e32 v24, 0x42800000, v68
	v_med3_f32 v23, v25, s33, v19
	v_med3_f32 v24, v24, s33, v19
	v_cvt_pk_fp8_f32 v26, v23, v24 op_sel:[0,0,1]
	v_mul_f32_e32 v23, 0x42800000, v57
	v_mul_f32_e32 v24, 0x42800000, v61
	v_med3_f32 v23, v23, s33, v19
	v_med3_f32 v24, v24, s33, v19
	v_mov_b32_e32 v27, 0
	v_cvt_pk_fp8_f32 v27, v23, v24
	v_mul_f32_e32 v25, 0x42800000, v65
	v_mul_f32_e32 v24, 0x42800000, v69
	v_med3_f32 v23, v25, s33, v19
	v_med3_f32 v24, v24, s33, v19
	v_cvt_pk_fp8_f32 v27, v23, v24 op_sel:[0,0,1]
	v_mul_f32_e32 v23, 0x42800000, v58
	v_mul_f32_e32 v24, 0x42800000, v62
	v_med3_f32 v23, v23, s33, v19
	v_med3_f32 v24, v24, s33, v19
	v_mov_b32_e32 v28, 0
	v_cvt_pk_fp8_f32 v28, v23, v24
	v_mul_f32_e32 v25, 0x42800000, v66
	v_mul_f32_e32 v24, 0x42800000, v70
	v_med3_f32 v23, v25, s33, v19
	v_med3_f32 v24, v24, s33, v19
	v_cvt_pk_fp8_f32 v28, v23, v24 op_sel:[0,0,1]
	v_mul_f32_e32 v23, 0x42800000, v59
	v_mul_f32_e32 v24, 0x42800000, v63
	v_med3_f32 v23, v23, s33, v19
	v_med3_f32 v24, v24, s33, v19
	v_mov_b32_e32 v29, 0
	v_cvt_pk_fp8_f32 v29, v23, v24
	v_mul_f32_e32 v25, 0x42800000, v67
	v_mul_f32_e32 v24, 0x42800000, v71
	v_med3_f32 v23, v25, s33, v19
	v_med3_f32 v24, v24, s33, v19
	s_waitcnt vmcnt(3)
	v_mul_f32_e32 v4, 0x42800000, v4
	s_waitcnt vmcnt(2)
	v_mul_f32_e32 v0, 0x42800000, v0
	v_cvt_pk_fp8_f32 v29, v23, v24 op_sel:[0,0,1]
	v_med3_f32 v4, v4, s33, v19
	v_med3_f32 v0, v0, s33, v19
	v_mov_b32_e32 v24, 0
	v_cvt_pk_fp8_f32 v24, v4, v0
	s_waitcnt vmcnt(1)
	v_mul_f32_e32 v23, 0x42800000, v72
	s_waitcnt vmcnt(0)
	v_mul_f32_e32 v4, 0x42800000, v76
	v_med3_f32 v0, v23, s33, v19
	v_med3_f32 v4, v4, s33, v19
	v_cvt_pk_fp8_f32 v24, v0, v4 op_sel:[0,0,1]
	v_mul_f32_e32 v0, 0x42800000, v5
	v_mul_f32_e32 v1, 0x42800000, v1
	v_med3_f32 v0, v0, s33, v19
	v_med3_f32 v1, v1, s33, v19
	v_mov_b32_e32 v5, 0
	v_cvt_pk_fp8_f32 v5, v0, v1
	v_mul_f32_e32 v4, 0x42800000, v73
	v_mul_f32_e32 v1, 0x42800000, v77
	v_med3_f32 v0, v4, s33, v19
	v_med3_f32 v1, v1, s33, v19
	v_cvt_pk_fp8_f32 v5, v0, v1 op_sel:[0,0,1]
	v_mul_f32_e32 v0, 0x42800000, v6
	v_mul_f32_e32 v1, 0x42800000, v2
	v_med3_f32 v0, v0, s33, v19
	v_med3_f32 v1, v1, s33, v19
	v_mov_b32_e32 v4, 0
	v_cvt_pk_fp8_f32 v4, v0, v1
	v_mul_f32_e32 v2, 0x42800000, v74
	v_mul_f32_e32 v1, 0x42800000, v78
	v_med3_f32 v0, v2, s33, v19
	v_med3_f32 v1, v1, s33, v19
	v_cvt_pk_fp8_f32 v4, v0, v1 op_sel:[0,0,1]
	v_mul_f32_e32 v0, 0x42800000, v7
	v_mul_f32_e32 v1, 0x42800000, v3
	v_med3_f32 v0, v0, s33, v19
	v_med3_f32 v1, v1, s33, v19
	v_mov_b32_e32 v3, 0
	v_cvt_pk_fp8_f32 v3, v0, v1
	v_mul_f32_e32 v2, 0x42800000, v75
	v_mul_f32_e32 v1, 0x42800000, v79
	v_med3_f32 v0, v2, s33, v19
	v_med3_f32 v1, v1, s33, v19
	v_cvt_pk_fp8_f32 v3, v0, v1 op_sel:[0,0,1]
	ds_write2_b32 v15, v26, v24 offset0:16 offset1:24
	ds_write2_b32 v15, v27, v5 offset0:50 offset1:58
	ds_write2_b32 v15, v28, v4 offset0:84 offset1:92
	ds_write2_b32 v15, v29, v3 offset0:118 offset1:126
	s_ashr_i32 s12, s34, 2
	s_and_b32 s15, s20, 0x60
	s_waitcnt lgkmcnt(0)
	s_mul_hi_i32 s21, s18, s12
	s_mul_i32 s12, s18, s12
	v_or_b32_e32 v4, s15, v14
	ds_read2_b64 v[0:3], v20 offset1:1
	v_or_b32_e32 v4, s12, v4
	v_mov_b64_e32 v[24:25], s[22:23]
	v_mad_u64_u32 v[4:5], s[18:19], v4, s14, v[24:25]
	v_mov_b32_e32 v23, s14
	v_mad_i32_i24 v5, s21, v23, v5
	s_ashr_i32 s17, s16, 31
	v_lshl_add_u64 v[4:5], v[4:5], 0, s[16:17]
	v_lshl_add_u64 v[26:27], v[4:5], 0, v[8:9]
	ds_read2_b64 v[4:7], v20 offset0:136 offset1:137
	s_waitcnt lgkmcnt(1)
	global_store_dwordx4 v[26:27], v[0:3], off sc1 nt
	s_add_i32 s30, s30, s31
	s_cmp_lt_i32 s30, 0x8400
	v_or_b32_e32 v0, s15, v16
	v_or_b32_e32 v0, s12, v0
	v_mad_u64_u32 v[0:1], s[18:19], v0, s14, v[24:25]
	v_mad_i32_i24 v1, s21, v23, v1
	v_lshl_add_u64 v[0:1], v[0:1], 0, s[16:17]
	v_lshl_add_u64 v[0:1], v[0:1], 0, v[8:9]
	s_waitcnt lgkmcnt(0)
	global_store_dwordx4 v[0:1], v[4:7], off sc1 nt
	ds_read2_b64 v[0:3], v21 offset1:1
	s_nop 0
	v_or_b32_e32 v4, s15, v17
	v_or_b32_e32 v4, s12, v4
	v_mad_u64_u32 v[4:5], s[18:19], v4, s14, v[24:25]
	v_mad_i32_i24 v5, s21, v23, v5
	v_lshl_add_u64 v[4:5], v[4:5], 0, s[16:17]
	v_lshl_add_u64 v[26:27], v[4:5], 0, v[8:9]
	ds_read2_b64 v[4:7], v22 offset1:1
	s_waitcnt lgkmcnt(1)
	global_store_dwordx4 v[26:27], v[0:3], off sc1 nt
	s_nop 1
	v_or_b32_e32 v0, s15, v18
	v_or_b32_e32 v0, s12, v0
	v_mad_u64_u32 v[0:1], s[14:15], v0, s14, v[24:25]
	v_mad_i32_i24 v1, s21, v23, v1
	v_lshl_add_u64 v[0:1], v[0:1], 0, s[16:17]
	v_lshl_add_u64 v[0:1], v[0:1], 0, v[8:9]
	s_waitcnt lgkmcnt(0)
	global_store_dwordx4 v[0:1], v[4:7], off sc1 nt
	s_waitcnt lgkmcnt(0)
	s_cbranch_scc0 .LBB0_723
